# down-projection epilogue: repeated per-row vmcnt waits (which drained the previous row's stores) removed in row blocks 1..7; router epilogue 1/rms loads batched
# baseline (speedup 1.0000x reference)
;     __device__ __forceinline__ void operator()(const f32x4 (&acc)[2][2][4][2], const Unit& u, int wr, int wc, int fr, int fq) const {
;         if (wc != 0) return;
;         const float* cb = cbr + (u.a0 >= 64 ? 32 : 0);
;         float* lg = (float*)u.O; const f32x4 b0 = *(const f32x4*)(br + 8 * fq) + *(const f32x4*)(cb + 8 * fq), b1 = *(const f32x4*)(br + 8 * fq + 4) + *(const f32x4*)(cb + 8 * fq + 4);
; #pragma unroll
;         for (int ai = 0; ai < 2; ++ai)
; #pragma unroll
;             for (int m = 0; m < 4; ++m) { const int rl = wr * 64 + fr + ai * HALF + m * 16; const float sr = rstd[u.a0 * BM + rl]; float* rp = lg + (size_t)rl * NE + 8 * fq; *(f32x4*)rp = acc[ai][0][m][0] * sr + b0; *(f32x4*)(rp + 4) = acc[ai][0][m][1] * sr + b1; }
.LBB0_1107:
	s_cmp_gt_i32 s51, 63
	v_ashrrev_i32_e32 v65, 1, v64
	s_cselect_b32 s2, 0x80, 0
	v_and_b32_e32 v66, -8, v65
	s_add_u32 s2, s36, s2
	v_ashrrev_i32_e32 v67, 31, v66
	s_addc_u32 s3, s37, 0
	v_lshlrev_b64 v[70:71], 2, v[66:67]
	v_lshl_add_u64 v[66:67], s[28:29], 0, v[70:71]
	v_lshl_add_u64 v[72:73], s[2:3], 0, v[70:71]
	v_and_or_b32 v64, v64, 15, s46
	s_lshl_b32 s2, s51, 8
	global_load_dwordx4 v[90:93], v[66:67], off offset:16
	s_nop 0
	global_load_dwordx4 v[66:69], v[66:67], off
	s_nop 0
	global_load_dwordx4 v[94:97], v[72:73], off offset:16
	global_load_dwordx4 v[98:101], v[72:73], off
	v_add_u32_e32 v72, s2, v64
	v_ashrrev_i32_e32 v73, 31, v72
	v_lshl_add_u64 v[72:73], v[72:73], 2, s[10:11]
	global_load_dword v102, v[72:73], off
	global_load_dword v152, v[72:73], off offset:64
	global_load_dword v154, v[72:73], off offset:128
	global_load_dword v156, v[72:73], off offset:192
	global_load_dword v158, v[72:73], off offset:512
	global_load_dword v160, v[72:73], off offset:576
	global_load_dword v162, v[72:73], off offset:640
	global_load_dword v164, v[72:73], off offset:704
	v_or_b32_e32 v104, 16, v64
	v_ashrrev_i32_e32 v65, 31, v64
	v_add_u32_e32 v74, s2, v104
	v_lshlrev_b64 v[72:73], 7, v[64:65]
	v_lshl_add_u64 v[70:71], s[20:21], 0, v[70:71]
	v_ashrrev_i32_e32 v75, 31, v74
	v_lshl_add_u64 v[106:107], v[70:71], 0, v[72:73]
	v_lshl_add_u64 v[108:109], v[74:75], 2, s[10:11]
	v_ashrrev_i32_e32 v105, 31, v104
	s_waitcnt vmcnt(8)
	v_pk_add_f32 v[72:73], v[68:69], v[100:101]
	v_pk_add_f32 v[74:75], v[66:67], v[98:99]
	v_pk_add_f32 v[66:67], v[92:93], v[96:97]
	v_pk_add_f32 v[68:69], v[90:91], v[94:95]
	s_waitcnt vmcnt(7)
	v_pk_fma_f32 v[60:61], v[60:61], v[102:103], v[74:75] op_sel_hi:[1,0,1]
	v_pk_fma_f32 v[62:63], v[62:63], v[102:103], v[72:73] op_sel_hi:[1,0,1]
	v_pk_fma_f32 v[56:57], v[56:57], v[102:103], v[68:69] op_sel_hi:[1,0,1]
	v_pk_fma_f32 v[58:59], v[58:59], v[102:103], v[66:67] op_sel_hi:[1,0,1]
	global_store_dwordx4 v[106:107], v[60:63], off
	global_store_dwordx4 v[106:107], v[56:59], off offset:16
	s_nop 0
	v_lshlrev_b64 v[60:61], 7, v[104:105]
	v_or_b32_e32 v58, 32, v64
	v_add_u32_e32 v62, s2, v58
	v_lshl_add_u64 v[60:61], v[70:71], 0, v[60:61]
	v_ashrrev_i32_e32 v63, 31, v62
	v_lshl_add_u64 v[62:63], v[62:63], 2, s[10:11]
	v_ashrrev_i32_e32 v59, 31, v58
	s_waitcnt vmcnt(8)
	v_pk_fma_f32 v[54:55], v[54:55], v[152:153], v[72:73] op_sel_hi:[1,0,1]
	v_pk_fma_f32 v[52:53], v[52:53], v[152:153], v[74:75] op_sel_hi:[1,0,1]
	v_pk_fma_f32 v[50:51], v[50:51], v[152:153], v[66:67] op_sel_hi:[1,0,1]
	v_pk_fma_f32 v[48:49], v[48:49], v[152:153], v[68:69] op_sel_hi:[1,0,1]
	global_store_dwordx4 v[60:61], v[52:55], off
	global_store_dwordx4 v[60:61], v[48:51], off offset:16
	s_nop 0
	v_lshlrev_b64 v[52:53], 7, v[58:59]
	v_or_b32_e32 v50, 48, v64
	v_add_u32_e32 v54, s2, v50
	v_lshl_add_u64 v[52:53], v[70:71], 0, v[52:53]
	v_ashrrev_i32_e32 v55, 31, v54
	v_lshl_add_u64 v[54:55], v[54:55], 2, s[10:11]
	v_ashrrev_i32_e32 v51, 31, v50
	s_waitcnt vmcnt(9)
	v_pk_fma_f32 v[46:47], v[46:47], v[154:155], v[72:73] op_sel_hi:[1,0,1]
	v_pk_fma_f32 v[44:45], v[44:45], v[154:155], v[74:75] op_sel_hi:[1,0,1]
	v_pk_fma_f32 v[42:43], v[42:43], v[154:155], v[66:67] op_sel_hi:[1,0,1]
	v_pk_fma_f32 v[40:41], v[40:41], v[154:155], v[68:69] op_sel_hi:[1,0,1]
	global_store_dwordx4 v[52:53], v[44:47], off
	global_store_dwordx4 v[52:53], v[40:43], off offset:16
	s_nop 0
	v_lshlrev_b64 v[44:45], 7, v[50:51]
	v_add_u32_e32 v42, 0x80, v64
	v_add_u32_e32 v46, s2, v42
	v_lshl_add_u64 v[44:45], v[70:71], 0, v[44:45]
	v_ashrrev_i32_e32 v47, 31, v46
	v_lshl_add_u64 v[46:47], v[46:47], 2, s[10:11]
	v_ashrrev_i32_e32 v43, 31, v42
	s_waitcnt vmcnt(10)
	v_pk_fma_f32 v[38:39], v[38:39], v[156:157], v[72:73] op_sel_hi:[1,0,1]
	v_pk_fma_f32 v[36:37], v[36:37], v[156:157], v[74:75] op_sel_hi:[1,0,1]
	v_pk_fma_f32 v[34:35], v[34:35], v[156:157], v[66:67] op_sel_hi:[1,0,1]
	v_pk_fma_f32 v[32:33], v[32:33], v[156:157], v[68:69] op_sel_hi:[1,0,1]
	global_store_dwordx4 v[44:45], v[36:39], off
	global_store_dwordx4 v[44:45], v[32:35], off offset:16
	s_nop 0
	v_lshlrev_b64 v[36:37], 7, v[42:43]
	v_add_u32_e32 v34, 0x90, v64
	v_add_u32_e32 v38, s2, v34
	v_lshl_add_u64 v[36:37], v[70:71], 0, v[36:37]
	v_ashrrev_i32_e32 v39, 31, v38
	v_lshl_add_u64 v[38:39], v[38:39], 2, s[10:11]
	v_ashrrev_i32_e32 v35, 31, v34
	s_waitcnt vmcnt(11)
	v_pk_fma_f32 v[30:31], v[30:31], v[158:159], v[72:73] op_sel_hi:[1,0,1]
	v_pk_fma_f32 v[28:29], v[28:29], v[158:159], v[74:75] op_sel_hi:[1,0,1]
	v_pk_fma_f32 v[26:27], v[26:27], v[158:159], v[66:67] op_sel_hi:[1,0,1]
	v_pk_fma_f32 v[24:25], v[24:25], v[158:159], v[68:69] op_sel_hi:[1,0,1]
	global_store_dwordx4 v[36:37], v[28:31], off
	global_store_dwordx4 v[36:37], v[24:27], off offset:16
	s_nop 0
	v_lshlrev_b64 v[28:29], 7, v[34:35]
	v_add_u32_e32 v26, 0xa0, v64
	v_add_u32_e32 v30, s2, v26
	v_lshl_add_u64 v[28:29], v[70:71], 0, v[28:29]
	v_ashrrev_i32_e32 v31, 31, v30
	v_lshl_add_u64 v[30:31], v[30:31], 2, s[10:11]
	v_ashrrev_i32_e32 v27, 31, v26
	s_waitcnt vmcnt(12)
	v_pk_fma_f32 v[22:23], v[22:23], v[160:161], v[72:73] op_sel_hi:[1,0,1]
	v_pk_fma_f32 v[20:21], v[20:21], v[160:161], v[74:75] op_sel_hi:[1,0,1]
	v_pk_fma_f32 v[18:19], v[18:19], v[160:161], v[66:67] op_sel_hi:[1,0,1]
	v_pk_fma_f32 v[16:17], v[16:17], v[160:161], v[68:69] op_sel_hi:[1,0,1]
	global_store_dwordx4 v[28:29], v[20:23], off
	global_store_dwordx4 v[28:29], v[16:19], off offset:16
	s_nop 0
	v_lshlrev_b64 v[20:21], 7, v[26:27]
	v_add_u32_e32 v18, 0xb0, v64
	v_add_u32_e32 v22, s2, v18
	v_lshl_add_u64 v[20:21], v[70:71], 0, v[20:21]
	v_ashrrev_i32_e32 v23, 31, v22
	v_lshl_add_u64 v[22:23], v[22:23], 2, s[10:11]
	v_ashrrev_i32_e32 v19, 31, v18
	s_waitcnt vmcnt(13)
	v_pk_fma_f32 v[14:15], v[14:15], v[162:163], v[72:73] op_sel_hi:[1,0,1]
	v_pk_fma_f32 v[12:13], v[12:13], v[162:163], v[74:75] op_sel_hi:[1,0,1]
	v_pk_fma_f32 v[10:11], v[10:11], v[162:163], v[66:67] op_sel_hi:[1,0,1]
	v_pk_fma_f32 v[8:9], v[8:9], v[162:163], v[68:69] op_sel_hi:[1,0,1]
	global_store_dwordx4 v[20:21], v[12:15], off
	global_store_dwordx4 v[20:21], v[8:11], off offset:16
	s_waitcnt vmcnt(14)
	v_pk_fma_f32 v[6:7], v[6:7], v[164:165], v[72:73] op_sel_hi:[1,0,1]
	v_lshlrev_b64 v[10:11], 7, v[18:19]
	v_lshl_add_u64 v[10:11], v[70:71], 0, v[10:11]
	v_pk_fma_f32 v[4:5], v[4:5], v[164:165], v[74:75] op_sel_hi:[1,0,1]
	v_pk_fma_f32 v[2:3], v[2:3], v[164:165], v[66:67] op_sel_hi:[1,0,1]
	v_pk_fma_f32 v[0:1], v[0:1], v[164:165], v[68:69] op_sel_hi:[1,0,1]
	global_store_dwordx4 v[10:11], v[4:7], off
	global_store_dwordx4 v[10:11], v[0:3], off offset:16
	s_andn2_b64 vcc, exec, s[18:19]
	s_mov_b64 s[2:3], -1
	s_cbranch_vccnz .LBB0_1098

; DI unsigned pk4f8(float a, float b, float c, float d) { int p = __builtin_amdgcn_cvt_pk_fp8_f32(a, b, 0, false); p = __builtin_amdgcn_cvt_pk_fp8_f32(c, d, p, true); return (unsigned)p; }
;     __device__ __forceinline__ void operator()(const f32x4 (&acc)[2][2][4][2], const Unit& u, int wr, int wc, int fr, int fq) const {
;     ...
;         const int row0 = wr * 64 + fr;
; #pragma unroll
;         for (int ai = 0; ai < 2; ++ai)
; #pragma unroll
;             for (int m = 0; m < 4; ++m) { const int r = row0 + ai * HALF + m * 16;
;                 if (r < valid) { const int slot = slots[r]; const float w = wts[r]; unsigned char* rowp = ys + (size_t)slot * D + col0;
; #pragma unroll
;                     for (int bj = 0; bj < 2; ++bj) { const f32x4 v0 = (acc[ai][bj][m][0] * WSCALE_INV + bv[bj][0]) * w, v1 = (acc[ai][bj][m][1] * WSCALE_INV + bv[bj][1]) * w;
;                         u32x2 o; o.x = pk4f8(v0[0], v0[1], v0[2], v0[3]); o.y = pk4f8(v1[0], v1[1], v1[2], v1[3]);
;                         *(u32x2*)(rowp + bj * HALF) = o; } } }
.LBB0_1340:
	s_or_b64 exec, exec, s[2:3]
	v_or_b32_e32 v112, 16, v160
	v_cmp_gt_i32_e32 vcc, s30, v112
	s_and_saveexec_b64 s[2:3], vcc
	s_cbranch_execz .LBB0_1342
	ds_read_b32 v112, v159 offset:64
	ds_read_b32 v114, v158 offset:64
	v_pk_fma_f32 v[104:105], v[104:105], s[16:17], v[136:137] op_sel_hi:[1,0,1]
	v_mov_b32_e32 v117, 0
	v_pk_fma_f32 v[108:109], v[108:109], s[16:17], v[140:141] op_sel_hi:[1,0,1]
	v_mov_b32_e32 v116, 0
	s_waitcnt lgkmcnt(0)
	v_pk_mul_f32 v[104:105], v[104:105], v[114:115] op_sel_hi:[1,0]
	v_pk_mul_f32 v[108:109], v[108:109], v[114:115] op_sel_hi:[1,0]
	v_cvt_pk_fp8_f32 v117, v104, v105
	v_pk_fma_f32 v[104:105], v[106:107], s[16:17], v[138:139] op_sel_hi:[1,0,1]
	v_pk_fma_f32 v[100:101], v[100:101], s[16:17], v[132:133] op_sel_hi:[1,0,1]
	v_pk_mul_f32 v[104:105], v[104:105], v[114:115] op_sel_hi:[1,0]
	v_pk_fma_f32 v[96:97], v[96:97], s[16:17], v[128:129] op_sel_hi:[1,0,1]
	v_cvt_pk_fp8_f32 v116, v108, v109
	v_cvt_pk_fp8_f32 v117, v104, v105 op_sel:[0,0,1]
	v_pk_mul_f32 v[100:101], v[100:101], v[114:115] op_sel_hi:[1,0]
	v_pk_mul_f32 v[96:97], v[96:97], v[114:115] op_sel_hi:[1,0]
	v_mov_b32_e32 v104, 0
	v_mov_b32_e32 v105, 0
	v_cvt_pk_fp8_f32 v104, v100, v101
	v_cvt_pk_fp8_f32 v105, v96, v97
	v_pk_fma_f32 v[110:111], v[110:111], s[16:17], v[142:143] op_sel_hi:[1,0,1]
	v_pk_fma_f32 v[102:103], v[102:103], s[16:17], v[134:135] op_sel_hi:[1,0,1]
	v_pk_mul_f32 v[110:111], v[110:111], v[114:115] op_sel_hi:[1,0]
	v_pk_fma_f32 v[96:97], v[98:99], s[16:17], v[130:131] op_sel_hi:[1,0,1]
	v_ashrrev_i32_e32 v113, 31, v112
	v_cvt_pk_fp8_f32 v116, v110, v111 op_sel:[0,0,1]
	v_pk_mul_f32 v[102:103], v[102:103], v[114:115] op_sel_hi:[1,0]
	v_pk_mul_f32 v[96:97], v[96:97], v[114:115] op_sel_hi:[1,0]
	v_lshlrev_b64 v[112:113], 11, v[112:113]
	v_cvt_pk_fp8_f32 v104, v102, v103 op_sel:[0,0,1]
	v_cvt_pk_fp8_f32 v105, v96, v97 op_sel:[0,0,1]
	v_lshl_add_u64 v[96:97], s[12:13], 0, v[112:113]
	v_lshl_add_u64 v[96:97], v[96:97], 0, v[144:145]
	global_store_dwordx2 v[96:97], v[116:117], off
	global_store_dwordx2 v[96:97], v[104:105], off offset:128
.LBB0_1342:
	s_or_b64 exec, exec, s[2:3]
	v_or_b32_e32 v96, 32, v160
	v_cmp_gt_i32_e32 vcc, s30, v96
	s_and_saveexec_b64 s[2:3], vcc
	s_cbranch_execz .LBB0_1344
	ds_read_b32 v96, v159 offset:128
	ds_read_b32 v98, v158 offset:128
	v_pk_fma_f32 v[88:89], v[88:89], s[16:17], v[136:137] op_sel_hi:[1,0,1]
	v_mov_b32_e32 v101, 0
	v_pk_fma_f32 v[92:93], v[92:93], s[16:17], v[140:141] op_sel_hi:[1,0,1]
	v_mov_b32_e32 v100, 0
	s_waitcnt lgkmcnt(0)
	v_pk_mul_f32 v[88:89], v[88:89], v[98:99] op_sel_hi:[1,0]
	v_pk_mul_f32 v[92:93], v[92:93], v[98:99] op_sel_hi:[1,0]
	v_cvt_pk_fp8_f32 v101, v88, v89
	v_pk_fma_f32 v[88:89], v[90:91], s[16:17], v[138:139] op_sel_hi:[1,0,1]
	v_pk_fma_f32 v[84:85], v[84:85], s[16:17], v[132:133] op_sel_hi:[1,0,1]
	v_pk_mul_f32 v[88:89], v[88:89], v[98:99] op_sel_hi:[1,0]
	v_pk_fma_f32 v[80:81], v[80:81], s[16:17], v[128:129] op_sel_hi:[1,0,1]
	v_cvt_pk_fp8_f32 v100, v92, v93
	v_cvt_pk_fp8_f32 v101, v88, v89 op_sel:[0,0,1]
	v_pk_mul_f32 v[84:85], v[84:85], v[98:99] op_sel_hi:[1,0]
	v_pk_mul_f32 v[80:81], v[80:81], v[98:99] op_sel_hi:[1,0]
	v_mov_b32_e32 v88, 0
	v_mov_b32_e32 v89, 0
	v_cvt_pk_fp8_f32 v88, v84, v85
	v_cvt_pk_fp8_f32 v89, v80, v81
	v_pk_fma_f32 v[94:95], v[94:95], s[16:17], v[142:143] op_sel_hi:[1,0,1]
	v_pk_fma_f32 v[86:87], v[86:87], s[16:17], v[134:135] op_sel_hi:[1,0,1]
	v_pk_mul_f32 v[94:95], v[94:95], v[98:99] op_sel_hi:[1,0]
	v_pk_fma_f32 v[80:81], v[82:83], s[16:17], v[130:131] op_sel_hi:[1,0,1]
	v_ashrrev_i32_e32 v97, 31, v96
	v_cvt_pk_fp8_f32 v100, v94, v95 op_sel:[0,0,1]
	v_pk_mul_f32 v[86:87], v[86:87], v[98:99] op_sel_hi:[1,0]
	v_pk_mul_f32 v[80:81], v[80:81], v[98:99] op_sel_hi:[1,0]
	v_lshlrev_b64 v[96:97], 11, v[96:97]
	v_cvt_pk_fp8_f32 v88, v86, v87 op_sel:[0,0,1]
	v_cvt_pk_fp8_f32 v89, v80, v81 op_sel:[0,0,1]
	v_lshl_add_u64 v[80:81], s[12:13], 0, v[96:97]
	v_lshl_add_u64 v[80:81], v[80:81], 0, v[144:145]
	global_store_dwordx2 v[80:81], v[100:101], off
	global_store_dwordx2 v[80:81], v[88:89], off offset:128
.LBB0_1344:
	s_or_b64 exec, exec, s[2:3]
	v_or_b32_e32 v80, 48, v160
	v_cmp_gt_i32_e32 vcc, s30, v80
	s_and_saveexec_b64 s[2:3], vcc
	s_cbranch_execz .LBB0_1346
	ds_read_b32 v80, v159 offset:192
	ds_read_b32 v82, v158 offset:192
	v_pk_fma_f32 v[72:73], v[72:73], s[16:17], v[136:137] op_sel_hi:[1,0,1]
	v_mov_b32_e32 v85, 0
	v_pk_fma_f32 v[76:77], v[76:77], s[16:17], v[140:141] op_sel_hi:[1,0,1]
	v_mov_b32_e32 v84, 0
	s_waitcnt lgkmcnt(0)
	v_pk_mul_f32 v[72:73], v[72:73], v[82:83] op_sel_hi:[1,0]
	v_pk_mul_f32 v[76:77], v[76:77], v[82:83] op_sel_hi:[1,0]
	v_cvt_pk_fp8_f32 v85, v72, v73
	v_pk_fma_f32 v[72:73], v[74:75], s[16:17], v[138:139] op_sel_hi:[1,0,1]
	v_pk_fma_f32 v[68:69], v[68:69], s[16:17], v[132:133] op_sel_hi:[1,0,1]
	v_pk_mul_f32 v[72:73], v[72:73], v[82:83] op_sel_hi:[1,0]
	v_pk_fma_f32 v[64:65], v[64:65], s[16:17], v[128:129] op_sel_hi:[1,0,1]
	v_cvt_pk_fp8_f32 v84, v76, v77
	v_cvt_pk_fp8_f32 v85, v72, v73 op_sel:[0,0,1]
	v_pk_mul_f32 v[68:69], v[68:69], v[82:83] op_sel_hi:[1,0]
	v_pk_mul_f32 v[64:65], v[64:65], v[82:83] op_sel_hi:[1,0]
	v_mov_b32_e32 v72, 0
	v_mov_b32_e32 v73, 0
	v_cvt_pk_fp8_f32 v72, v68, v69
	v_cvt_pk_fp8_f32 v73, v64, v65
	v_pk_fma_f32 v[78:79], v[78:79], s[16:17], v[142:143] op_sel_hi:[1,0,1]
	v_pk_fma_f32 v[70:71], v[70:71], s[16:17], v[134:135] op_sel_hi:[1,0,1]
	v_pk_mul_f32 v[78:79], v[78:79], v[82:83] op_sel_hi:[1,0]
	v_pk_fma_f32 v[64:65], v[66:67], s[16:17], v[130:131] op_sel_hi:[1,0,1]
	v_ashrrev_i32_e32 v81, 31, v80
	v_cvt_pk_fp8_f32 v84, v78, v79 op_sel:[0,0,1]
	v_pk_mul_f32 v[70:71], v[70:71], v[82:83] op_sel_hi:[1,0]
	v_pk_mul_f32 v[64:65], v[64:65], v[82:83] op_sel_hi:[1,0]
	v_lshlrev_b64 v[80:81], 11, v[80:81]
	v_cvt_pk_fp8_f32 v72, v70, v71 op_sel:[0,0,1]
	v_cvt_pk_fp8_f32 v73, v64, v65 op_sel:[0,0,1]
	v_lshl_add_u64 v[64:65], s[12:13], 0, v[80:81]
	v_lshl_add_u64 v[64:65], v[64:65], 0, v[144:145]
	global_store_dwordx2 v[64:65], v[84:85], off
	global_store_dwordx2 v[64:65], v[72:73], off offset:128
; DI unsigned pk4f8(float a, float b, float c, float d) { int p = __builtin_amdgcn_cvt_pk_fp8_f32(a, b, 0, false); p = __builtin_amdgcn_cvt_pk_fp8_f32(c, d, p, true); return (unsigned)p; }
;     __device__ __forceinline__ void operator()(const f32x4 (&acc)[2][2][4][2], const Unit& u, int wr, int wc, int fr, int fq) const {
;     ...
;         const int row0 = wr * 64 + fr;
; #pragma unroll
;         for (int ai = 0; ai < 2; ++ai)
; #pragma unroll
;             for (int m = 0; m < 4; ++m) { const int r = row0 + ai * HALF + m * 16;
;                 if (r < valid) { const int slot = slots[r]; const float w = wts[r]; unsigned char* rowp = ys + (size_t)slot * D + col0;
; #pragma unroll
;                     for (int bj = 0; bj < 2; ++bj) { const f32x4 v0 = (acc[ai][bj][m][0] * WSCALE_INV + bv[bj][0]) * w, v1 = (acc[ai][bj][m][1] * WSCALE_INV + bv[bj][1]) * w;
;                         u32x2 o; o.x = pk4f8(v0[0], v0[1], v0[2], v0[3]); o.y = pk4f8(v1[0], v1[1], v1[2], v1[3]);
;                         *(u32x2*)(rowp + bj * HALF) = o; } } }
.LBB0_1346:
	s_or_b64 exec, exec, s[2:3]
	v_add_u32_e32 v64, 0x80, v160
	v_cmp_gt_i32_e32 vcc, s30, v64
	s_and_saveexec_b64 s[2:3], vcc
	s_cbranch_execz .LBB0_1348
	ds_read_b32 v64, v159 offset:512
	ds_read_b32 v66, v158 offset:512
	v_pk_fma_f32 v[56:57], v[56:57], s[16:17], v[136:137] op_sel_hi:[1,0,1]
	v_mov_b32_e32 v69, 0
	v_pk_fma_f32 v[60:61], v[60:61], s[16:17], v[140:141] op_sel_hi:[1,0,1]
	v_mov_b32_e32 v68, 0
	s_waitcnt lgkmcnt(0)
	v_pk_mul_f32 v[56:57], v[56:57], v[66:67] op_sel_hi:[1,0]
	v_pk_mul_f32 v[60:61], v[60:61], v[66:67] op_sel_hi:[1,0]
	v_cvt_pk_fp8_f32 v69, v56, v57
	v_pk_fma_f32 v[56:57], v[58:59], s[16:17], v[138:139] op_sel_hi:[1,0,1]
	v_pk_fma_f32 v[52:53], v[52:53], s[16:17], v[132:133] op_sel_hi:[1,0,1]
	v_pk_mul_f32 v[56:57], v[56:57], v[66:67] op_sel_hi:[1,0]
	v_pk_fma_f32 v[48:49], v[48:49], s[16:17], v[128:129] op_sel_hi:[1,0,1]
	v_cvt_pk_fp8_f32 v68, v60, v61
	v_cvt_pk_fp8_f32 v69, v56, v57 op_sel:[0,0,1]
	v_pk_mul_f32 v[52:53], v[52:53], v[66:67] op_sel_hi:[1,0]
	v_pk_mul_f32 v[48:49], v[48:49], v[66:67] op_sel_hi:[1,0]
	v_mov_b32_e32 v56, 0
	v_mov_b32_e32 v57, 0
	v_cvt_pk_fp8_f32 v56, v52, v53
	v_cvt_pk_fp8_f32 v57, v48, v49
	v_pk_fma_f32 v[62:63], v[62:63], s[16:17], v[142:143] op_sel_hi:[1,0,1]
	v_pk_fma_f32 v[54:55], v[54:55], s[16:17], v[134:135] op_sel_hi:[1,0,1]
	v_pk_mul_f32 v[62:63], v[62:63], v[66:67] op_sel_hi:[1,0]
	v_pk_fma_f32 v[48:49], v[50:51], s[16:17], v[130:131] op_sel_hi:[1,0,1]
	v_ashrrev_i32_e32 v65, 31, v64
	v_cvt_pk_fp8_f32 v68, v62, v63 op_sel:[0,0,1]
	v_pk_mul_f32 v[54:55], v[54:55], v[66:67] op_sel_hi:[1,0]
	v_pk_mul_f32 v[48:49], v[48:49], v[66:67] op_sel_hi:[1,0]
	v_lshlrev_b64 v[64:65], 11, v[64:65]
	v_cvt_pk_fp8_f32 v56, v54, v55 op_sel:[0,0,1]
	v_cvt_pk_fp8_f32 v57, v48, v49 op_sel:[0,0,1]
	v_lshl_add_u64 v[48:49], s[12:13], 0, v[64:65]
	v_lshl_add_u64 v[48:49], v[48:49], 0, v[144:145]
	global_store_dwordx2 v[48:49], v[68:69], off
	global_store_dwordx2 v[48:49], v[56:57], off offset:128
.LBB0_1348:
	s_or_b64 exec, exec, s[2:3]
	v_add_u32_e32 v48, 0x90, v160
	v_cmp_gt_i32_e32 vcc, s30, v48
	s_and_saveexec_b64 s[2:3], vcc
	s_cbranch_execz .LBB0_1350
	ds_read_b32 v48, v159 offset:576
	ds_read_b32 v50, v158 offset:576
	v_pk_fma_f32 v[40:41], v[40:41], s[16:17], v[136:137] op_sel_hi:[1,0,1]
	v_mov_b32_e32 v53, 0
	v_pk_fma_f32 v[44:45], v[44:45], s[16:17], v[140:141] op_sel_hi:[1,0,1]
	v_mov_b32_e32 v52, 0
	s_waitcnt lgkmcnt(0)
	v_pk_mul_f32 v[40:41], v[40:41], v[50:51] op_sel_hi:[1,0]
	v_pk_mul_f32 v[44:45], v[44:45], v[50:51] op_sel_hi:[1,0]
	v_cvt_pk_fp8_f32 v53, v40, v41
	v_pk_fma_f32 v[40:41], v[42:43], s[16:17], v[138:139] op_sel_hi:[1,0,1]
	v_pk_fma_f32 v[36:37], v[36:37], s[16:17], v[132:133] op_sel_hi:[1,0,1]
	v_pk_mul_f32 v[40:41], v[40:41], v[50:51] op_sel_hi:[1,0]
	v_pk_fma_f32 v[32:33], v[32:33], s[16:17], v[128:129] op_sel_hi:[1,0,1]
	v_cvt_pk_fp8_f32 v52, v44, v45
	v_cvt_pk_fp8_f32 v53, v40, v41 op_sel:[0,0,1]
	v_pk_mul_f32 v[36:37], v[36:37], v[50:51] op_sel_hi:[1,0]
	v_pk_mul_f32 v[32:33], v[32:33], v[50:51] op_sel_hi:[1,0]
	v_mov_b32_e32 v40, 0
	v_mov_b32_e32 v41, 0
	v_cvt_pk_fp8_f32 v40, v36, v37
	v_cvt_pk_fp8_f32 v41, v32, v33
	v_pk_fma_f32 v[46:47], v[46:47], s[16:17], v[142:143] op_sel_hi:[1,0,1]
	v_pk_fma_f32 v[38:39], v[38:39], s[16:17], v[134:135] op_sel_hi:[1,0,1]
	v_pk_mul_f32 v[46:47], v[46:47], v[50:51] op_sel_hi:[1,0]
	v_pk_fma_f32 v[32:33], v[34:35], s[16:17], v[130:131] op_sel_hi:[1,0,1]
	v_ashrrev_i32_e32 v49, 31, v48
	v_cvt_pk_fp8_f32 v52, v46, v47 op_sel:[0,0,1]
	v_pk_mul_f32 v[38:39], v[38:39], v[50:51] op_sel_hi:[1,0]
	v_pk_mul_f32 v[32:33], v[32:33], v[50:51] op_sel_hi:[1,0]
	v_lshlrev_b64 v[48:49], 11, v[48:49]
	v_cvt_pk_fp8_f32 v40, v38, v39 op_sel:[0,0,1]
	v_cvt_pk_fp8_f32 v41, v32, v33 op_sel:[0,0,1]
	v_lshl_add_u64 v[32:33], s[12:13], 0, v[48:49]
	v_lshl_add_u64 v[32:33], v[32:33], 0, v[144:145]
	global_store_dwordx2 v[32:33], v[52:53], off
	global_store_dwordx2 v[32:33], v[40:41], off offset:128
; DI unsigned pk4f8(float a, float b, float c, float d) { int p = __builtin_amdgcn_cvt_pk_fp8_f32(a, b, 0, false); p = __builtin_amdgcn_cvt_pk_fp8_f32(c, d, p, true); return (unsigned)p; }
;     __device__ __forceinline__ void operator()(const f32x4 (&acc)[2][2][4][2], const Unit& u, int wr, int wc, int fr, int fq) const {
;     ...
;         const int row0 = wr * 64 + fr;
; #pragma unroll
;         for (int ai = 0; ai < 2; ++ai)
; #pragma unroll
;             for (int m = 0; m < 4; ++m) { const int r = row0 + ai * HALF + m * 16;
;                 if (r < valid) { const int slot = slots[r]; const float w = wts[r]; unsigned char* rowp = ys + (size_t)slot * D + col0;
; #pragma unroll
;                     for (int bj = 0; bj < 2; ++bj) { const f32x4 v0 = (acc[ai][bj][m][0] * WSCALE_INV + bv[bj][0]) * w, v1 = (acc[ai][bj][m][1] * WSCALE_INV + bv[bj][1]) * w;
;                         u32x2 o; o.x = pk4f8(v0[0], v0[1], v0[2], v0[3]); o.y = pk4f8(v1[0], v1[1], v1[2], v1[3]);
;                         *(u32x2*)(rowp + bj * HALF) = o; } } }
.LBB0_1350:
	s_or_b64 exec, exec, s[2:3]
	v_add_u32_e32 v32, 0xa0, v160
	v_cmp_gt_i32_e32 vcc, s30, v32
	s_and_saveexec_b64 s[2:3], vcc
	s_cbranch_execz .LBB0_1352
	ds_read_b32 v32, v159 offset:640
	ds_read_b32 v34, v158 offset:640
	v_pk_fma_f32 v[24:25], v[24:25], s[16:17], v[136:137] op_sel_hi:[1,0,1]
	v_mov_b32_e32 v37, 0
	v_pk_fma_f32 v[28:29], v[28:29], s[16:17], v[140:141] op_sel_hi:[1,0,1]
	v_mov_b32_e32 v36, 0
	s_waitcnt lgkmcnt(0)
	v_pk_mul_f32 v[24:25], v[24:25], v[34:35] op_sel_hi:[1,0]
	v_pk_mul_f32 v[28:29], v[28:29], v[34:35] op_sel_hi:[1,0]
	v_cvt_pk_fp8_f32 v37, v24, v25
	v_pk_fma_f32 v[24:25], v[26:27], s[16:17], v[138:139] op_sel_hi:[1,0,1]
	v_pk_fma_f32 v[20:21], v[20:21], s[16:17], v[132:133] op_sel_hi:[1,0,1]
	v_pk_mul_f32 v[24:25], v[24:25], v[34:35] op_sel_hi:[1,0]
	v_pk_fma_f32 v[16:17], v[16:17], s[16:17], v[128:129] op_sel_hi:[1,0,1]
	v_cvt_pk_fp8_f32 v36, v28, v29
	v_cvt_pk_fp8_f32 v37, v24, v25 op_sel:[0,0,1]
	v_pk_mul_f32 v[20:21], v[20:21], v[34:35] op_sel_hi:[1,0]
	v_pk_mul_f32 v[16:17], v[16:17], v[34:35] op_sel_hi:[1,0]
	v_mov_b32_e32 v24, 0
	v_mov_b32_e32 v25, 0
	v_cvt_pk_fp8_f32 v24, v20, v21
	v_cvt_pk_fp8_f32 v25, v16, v17
	v_pk_fma_f32 v[30:31], v[30:31], s[16:17], v[142:143] op_sel_hi:[1,0,1]
	v_pk_fma_f32 v[22:23], v[22:23], s[16:17], v[134:135] op_sel_hi:[1,0,1]
	v_pk_mul_f32 v[30:31], v[30:31], v[34:35] op_sel_hi:[1,0]
	v_pk_fma_f32 v[16:17], v[18:19], s[16:17], v[130:131] op_sel_hi:[1,0,1]
	v_ashrrev_i32_e32 v33, 31, v32
	v_cvt_pk_fp8_f32 v36, v30, v31 op_sel:[0,0,1]
	v_pk_mul_f32 v[22:23], v[22:23], v[34:35] op_sel_hi:[1,0]
	v_pk_mul_f32 v[16:17], v[16:17], v[34:35] op_sel_hi:[1,0]
	v_lshlrev_b64 v[32:33], 11, v[32:33]
	v_cvt_pk_fp8_f32 v24, v22, v23 op_sel:[0,0,1]
	v_cvt_pk_fp8_f32 v25, v16, v17 op_sel:[0,0,1]
	v_lshl_add_u64 v[16:17], s[12:13], 0, v[32:33]
	v_lshl_add_u64 v[16:17], v[16:17], 0, v[144:145]
	global_store_dwordx2 v[16:17], v[36:37], off
	global_store_dwordx2 v[16:17], v[24:25], off offset:128
.LBB0_1352:
	s_or_b64 exec, exec, s[2:3]
	v_add_u32_e32 v16, 0xb0, v160
	v_cmp_gt_i32_e32 vcc, s30, v16
	s_and_saveexec_b64 s[2:3], vcc
	s_cbranch_execz .LBB0_1354
	ds_read_b32 v16, v159 offset:704
	ds_read_b32 v18, v158 offset:704
	v_pk_fma_f32 v[8:9], v[8:9], s[16:17], v[136:137] op_sel_hi:[1,0,1]
	v_mov_b32_e32 v21, 0
	v_pk_fma_f32 v[12:13], v[12:13], s[16:17], v[140:141] op_sel_hi:[1,0,1]
	v_mov_b32_e32 v20, 0
	s_waitcnt lgkmcnt(0)
	v_pk_mul_f32 v[8:9], v[8:9], v[18:19] op_sel_hi:[1,0]
	v_pk_mul_f32 v[12:13], v[12:13], v[18:19] op_sel_hi:[1,0]
	v_cvt_pk_fp8_f32 v21, v8, v9
	v_pk_fma_f32 v[8:9], v[10:11], s[16:17], v[138:139] op_sel_hi:[1,0,1]
	v_pk_fma_f32 v[4:5], v[4:5], s[16:17], v[132:133] op_sel_hi:[1,0,1]
	v_pk_mul_f32 v[8:9], v[8:9], v[18:19] op_sel_hi:[1,0]
	v_pk_fma_f32 v[0:1], v[0:1], s[16:17], v[128:129] op_sel_hi:[1,0,1]
	v_cvt_pk_fp8_f32 v20, v12, v13
	v_cvt_pk_fp8_f32 v21, v8, v9 op_sel:[0,0,1]
	v_pk_mul_f32 v[4:5], v[4:5], v[18:19] op_sel_hi:[1,0]
	v_pk_mul_f32 v[0:1], v[0:1], v[18:19] op_sel_hi:[1,0]
	v_mov_b32_e32 v8, 0
	v_mov_b32_e32 v9, 0
	v_cvt_pk_fp8_f32 v8, v4, v5
	v_cvt_pk_fp8_f32 v9, v0, v1
	v_pk_fma_f32 v[14:15], v[14:15], s[16:17], v[142:143] op_sel_hi:[1,0,1]
	v_pk_fma_f32 v[6:7], v[6:7], s[16:17], v[134:135] op_sel_hi:[1,0,1]
	v_pk_mul_f32 v[14:15], v[14:15], v[18:19] op_sel_hi:[1,0]
	v_pk_fma_f32 v[0:1], v[2:3], s[16:17], v[130:131] op_sel_hi:[1,0,1]
	v_ashrrev_i32_e32 v17, 31, v16
	v_cvt_pk_fp8_f32 v20, v14, v15 op_sel:[0,0,1]
	v_pk_mul_f32 v[6:7], v[6:7], v[18:19] op_sel_hi:[1,0]
	v_pk_mul_f32 v[0:1], v[0:1], v[18:19] op_sel_hi:[1,0]
	v_lshlrev_b64 v[16:17], 11, v[16:17]
	v_cvt_pk_fp8_f32 v8, v6, v7 op_sel:[0,0,1]
	v_cvt_pk_fp8_f32 v9, v0, v1 op_sel:[0,0,1]
	v_lshl_add_u64 v[0:1], s[12:13], 0, v[16:17]
	v_lshl_add_u64 v[0:1], v[0:1], 0, v[144:145]
	global_store_dwordx2 v[0:1], v[20:21], off
	global_store_dwordx2 v[0:1], v[8:9], off offset:128
